# grid barrier after E(l>=1): leader skips the L2 write-back (phase outputs are write-through or consumed a layer later)
# speedup vs baseline: 1.0062x; 1.0062x over previous
; __device__ __forceinline__ unsigned xb_add(unsigned* p, unsigned v) { return __hip_atomic_fetch_add(p, v, __ATOMIC_RELAXED, __HIP_MEMORY_SCOPE_AGENT); }
; __device__ __forceinline__ void xcd_barrier(const XcdBarrier& b) {
;     ...
;         const unsigned old = xb_add(&bar[XB_XSUB(b.x)], 1u);
;         const unsigned gen = old / nloc;
;         if (old + 1u == (gen + 1u) * nloc) {
;             __builtin_amdgcn_fence(__ATOMIC_RELEASE, "agent");
;             asm volatile("s_waitcnt vmcnt(0)" ::: "memory");
;             const unsigned og = xb_add(&bar[XB_TOP], 1u);
.LBB0_1009:
	s_andn2_saveexec_b64 s[2:3], s[2:3]
	s_cbranch_execz .LBB0_1029
	s_mov_b64 s[2:3], exec
	v_readlane_b32 s24, v255, 35
	s_nop 3
	s_cmp_eq_u32 s24, 6
	s_cbranch_scc1 .Lxb_nowb
	s_cmp_eq_u32 s24, 12
	s_cbranch_scc1 .Lxb_nowb
	s_cmp_eq_u32 s24, 18
	s_cbranch_scc1 .Lxb_nowb
	buffer_wbl2 sc1
.Lxb_nowb:
	s_waitcnt lgkmcnt(0)
	s_waitcnt vmcnt(0)
	v_mbcnt_lo_u32_b32 v1, s2, 0
	v_mbcnt_hi_u32_b32 v1, s3, v1
	v_cmp_eq_u32_e32 vcc, 0, v1
	s_and_saveexec_b64 s[20:21], vcc
	s_cbranch_execz .LBB0_1012
	s_bcnt1_i32_b64 s2, s[2:3]
	v_mov_b32_e32 v4, s2
	v_readlane_b32 s2, v255, 25
	v_readlane_b32 s3, v255, 26
	s_nop 4
	global_atomic_add v4, v3, v4, s[2:3] sc0
